# speedup vs baseline: 1.0047x; 1.0047x over previous
_Z10kvq_kernelPKtS0_PtS1_S1_PKf:
	s_ashr_i32 s3, s2, 31
	s_lshr_b32 s3, s3, 29
	s_add_i32 s3, s2, s3
	v_lshlrev_b32_e32 v1, 4, v0
	v_and_b32_e32 v2, 32, v0
	s_ashr_i32 s3, s3, 3
	v_bitop3_b32 v1, v1, v2, 48 bitop3:0x6c
	v_lshrrev_b32_e32 v2, 1, v0
	v_lshrrev_b32_e32 v4, 5, v0
	s_lshl_b32 s2, s2, 5
	s_mul_i32 s12, s3, 0xffffff01
	v_and_b32_e32 v2, 24, v2
	v_and_b32_e32 v4, 4, v4
	v_bfe_u32 v5, v0, 2, 2
	s_add_i32 s12, s12, s2
	v_bfe_u32 v3, v0, 2, 4
	v_or3_b32 v2, v4, v5, v2
	v_lshrrev_b32_e32 v4, 3, v0
	s_load_dwordx8 s[4:11], s[0:1], 0x0
	s_ashr_i32 s2, s12, 5
	s_and_b32 s13, s3, 7
	s_lshr_b32 s3, s3, 3
	v_and_or_b32 v1, v0, 64, v1
	v_and_or_b32 v5, v4, 48, v3
	v_and_or_b32 v4, v4, 32, v2
	s_lshl_b32 s12, s2, 3
	s_add_i32 s2, s2, s3
	v_lshl_or_b32 v84, v4, 11, v1
	v_bfe_u32 v4, v0, 3, 25
	s_or_b32 s14, s12, s13
	s_and_b32 s23, s2, 3
	v_or_b32_e32 v4, 64, v4
	s_movk_i32 s2, 0x70
	v_readfirstlane_b32 s18, v0
	v_and_or_b32 v3, v4, s2, v3
	s_movk_i32 s2, 0x60
	s_ashr_i32 s15, s14, 31
	s_lshr_b32 s16, s18, 8
	v_and_or_b32 v2, v4, s2, v2
	s_lshl_b64 s[2:3], s[14:15], 18
	s_waitcnt lgkmcnt(0)
	s_add_u32 s4, s4, s2
	s_addc_u32 s5, s5, s3
	s_lshr_b32 s2, s18, 1
	s_lshl_b32 s3, s18, 4
	s_and_b32 s3, s3, 0xfffffc00
	s_and_b32 s15, s2, 0x60
	s_lshl_b32 s2, s23, 19
	s_add_u32 s12, s6, s2
	s_addc_u32 s13, s7, 0
	s_add_i32 s19, s3, 0
	s_add_i32 m0, s19, 0x4000
	v_lshl_or_b32 v88, v2, 11, v1
	global_load_lds_dwordx4 v84, s[12:13]
	s_add_i32 m0, s19, 0x6000
	v_lshl_or_b32 v82, v5, 11, v1
	global_load_lds_dwordx4 v88, s[12:13]
	s_mov_b32 m0, s19
	s_add_u32 s2, s12, 0x40000
	v_mov_b32_e32 v2, 0
	global_load_lds_dwordx4 v82, s[4:5]
	s_addc_u32 s3, s13, 0
	s_add_i32 m0, s19, 0x8000
	v_mov_b32_e32 v85, v2
	global_load_lds_dwordx4 v84, s[2:3]
	s_add_i32 m0, s19, 0xa000
	v_lshl_or_b32 v86, v3, 11, v1
	v_lshl_add_u64 v[4:5], s[12:13], 0, v[84:85]
	v_mov_b32_e32 v89, v2
	global_load_lds_dwordx4 v88, s[2:3]
	s_add_i32 m0, s19, 0x2000
	s_mov_b64 s[2:3], 0x80
	v_lshl_add_u64 v[6:7], s[12:13], 0, v[88:89]
	global_load_lds_dwordx4 v86, s[4:5]
	v_lshl_add_u64 v[4:5], v[4:5], 0, s[2:3]
	s_add_i32 m0, s19, 0x10000
	v_mov_b32_e32 v83, v2
	global_load_lds_dwordx4 v[4:5], off
	v_lshl_add_u64 v[4:5], v[6:7], 0, s[2:3]
	s_add_i32 m0, s19, 0x12000
	v_lshl_add_u64 v[8:9], s[4:5], 0, v[82:83]
	global_load_lds_dwordx4 v[4:5], off
	s_add_i32 m0, s19, 0xc000
	v_lshl_add_u64 v[4:5], v[8:9], 0, s[2:3]
	s_add_u32 s20, s12, 0x40080
	v_mov_b32_e32 v87, v2
	global_load_lds_dwordx4 v[4:5], off
	s_addc_u32 s21, s13, 0
	s_add_i32 m0, s19, 0x14000
	v_lshl_add_u64 v[10:11], s[4:5], 0, v[86:87]
	global_load_lds_dwordx4 v84, s[20:21]
	s_add_i32 m0, s19, 0x16000
	v_lshl_add_u64 v[4:5], v[10:11], 0, s[2:3]
	global_load_lds_dwordx4 v88, s[20:21]
	s_add_i32 m0, s19, 0xe000
	s_load_dwordx4 s[0:3], s[0:1], 0x20
	global_load_lds_dwordx4 v[4:5], off
	s_lshl_b32 s20, s23, 10
	v_bfe_u32 v3, v0, 4, 2
	s_waitcnt lgkmcnt(0)
	s_add_u32 s20, s2, s20
	s_addc_u32 s21, s3, 0
	s_lshl_b32 s22, s15, 2
	s_add_u32 s26, s20, s22
	s_addc_u32 s27, s21, 0
	v_lshlrev_b32_e32 v4, 5, v3
	v_mov_b32_e32 v5, v2
	v_lshl_add_u64 v[4:5], s[26:27], 0, v[4:5]
	global_load_dwordx4 v[18:21], v[4:5], off
	global_load_dwordx4 v[14:17], v[4:5], off offset:16
	global_load_dwordx4 v[10:13], v[4:5], off offset:512
	global_load_dwordx4 v[6:9], v[4:5], off offset:528
	s_waitcnt vmcnt(10)
	v_lshlrev_b32_e32 v1, 3, v3
	s_mov_b32 s17, 0
	s_mov_b32 s24, 0xc000
	s_mov_b32 s3, 2
	s_cmp_lg_u32 s16, 1
	s_cbranch_scc1 .LBB1_2
	s_barrier

_Z11out2_kernelPKtS0_PfPKf:
	s_load_dwordx8 s[4:11], s[0:1], 0x0
	s_ashr_i32 s0, s2, 31
	s_lshr_b32 s0, s0, 29
	s_add_i32 s0, s2, s0
	s_ashr_i32 s1, s0, 3
	s_lshl_b32 s0, s2, 5
	s_mul_i32 s2, s1, 0xffffff01
	s_add_i32 s2, s2, s0
	s_ashr_i32 s0, s2, 2
	v_lshlrev_b32_e32 v1, 4, v0
	v_and_b32_e32 v2, 32, v0
	s_and_b32 s0, s0, -8
	s_and_b32 s2, s1, 7
	v_bfe_u32 v3, v0, 2, 4
	v_bitop3_b32 v1, v1, v2, 48 bitop3:0x6c
	v_lshrrev_b32_e32 v2, 3, v0
	s_or_b32 s0, s0, s2
	s_bfe_u32 s16, s1, 0x20003
	v_and_or_b32 v4, v2, 48, v3
	v_or_b32_e32 v2, 64, v2
	s_movk_i32 s1, 0x70
	v_readfirstlane_b32 s12, v0
	v_and_or_b32 v2, v2, s1, v3
	s_ashr_i32 s1, s0, 31
	s_lshr_b32 s14, s12, 8
	s_lshl_b64 s[2:3], s[0:1], 18
	s_waitcnt lgkmcnt(0)
	s_add_u32 s2, s4, s2
	s_addc_u32 s3, s5, s3
	s_lshr_b32 s1, s12, 1
	s_lshl_b32 s4, s12, 4
	s_and_b32 s13, s4, 0xfffffc00
	s_and_b32 s1, s1, 0x60
	s_lshl_b32 s4, s16, 19
	s_add_u32 s4, s6, s4
	v_and_or_b32 v1, v0, 64, v1
	s_addc_u32 s5, s7, 0
	s_add_i32 s6, s13, 0
	v_lshl_or_b32 v82, v4, 11, v1
	s_add_i32 m0, s6, 0x4000
	v_lshl_or_b32 v84, v2, 11, v1
	global_load_lds_dwordx4 v82, s[4:5]
	s_add_i32 m0, s6, 0x6000
	s_add_u32 s18, s4, 0x40000
	global_load_lds_dwordx4 v84, s[4:5]
	s_mov_b32 m0, s6
	v_mov_b32_e32 v18, 0
	global_load_lds_dwordx4 v82, s[2:3]
	s_addc_u32 s19, s5, 0
	s_add_i32 m0, s6, 0x8000
	v_mov_b32_e32 v83, v18
	global_load_lds_dwordx4 v82, s[18:19]
	s_add_i32 m0, s6, 0xa000
	v_lshl_add_u64 v[2:3], s[4:5], 0, v[82:83]
	v_mov_b32_e32 v85, v18
	global_load_lds_dwordx4 v84, s[18:19]
	s_add_i32 m0, s6, 0x2000
	s_mov_b64 s[18:19], 0x80
	v_lshl_add_u64 v[4:5], s[4:5], 0, v[84:85]
	global_load_lds_dwordx4 v84, s[2:3]
	v_lshl_add_u64 v[2:3], v[2:3], 0, s[18:19]
	s_add_i32 m0, s6, 0x10000
	v_lshl_add_u64 v[6:7], s[2:3], 0, v[82:83]
	global_load_lds_dwordx4 v[2:3], off
	v_lshl_add_u64 v[2:3], v[4:5], 0, s[18:19]
	s_add_i32 m0, s6, 0x12000
	v_lshl_add_u64 v[8:9], s[2:3], 0, v[84:85]
	global_load_lds_dwordx4 v[2:3], off
	s_add_i32 m0, s6, 0xc000
	v_lshl_add_u64 v[2:3], v[6:7], 0, s[18:19]
	s_add_u32 s20, s4, 0x40080
	global_load_lds_dwordx4 v[2:3], off
	s_addc_u32 s21, s5, 0
	s_add_i32 m0, s6, 0x14000
	v_lshl_add_u64 v[2:3], v[8:9], 0, s[18:19]
	global_load_lds_dwordx4 v82, s[20:21]
	s_add_i32 m0, s6, 0x16000
	s_lshl_b32 s17, s16, 10
	global_load_lds_dwordx4 v84, s[20:21]
	s_add_i32 m0, s6, 0xe000
	s_add_u32 s10, s10, s17
	global_load_lds_dwordx4 v[2:3], off
	s_addc_u32 s11, s11, 0
	s_lshl_b32 s17, s1, 2
	v_bfe_u32 v1, v0, 4, 2
	s_add_u32 s10, s10, s17
	s_addc_u32 s11, s11, 0
	v_lshlrev_b32_e32 v20, 4, v1
	v_mov_b32_e32 v21, v18
	v_lshl_add_u64 v[22:23], s[10:11], 0, v[20:21]
	global_load_dwordx4 v[14:17], v[22:23], off
	global_load_dwordx4 v[10:13], v[22:23], off offset:64
	global_load_dwordx4 v[6:9], v[22:23], off offset:512
	global_load_dwordx4 v[2:5], v[22:23], off offset:576
	s_waitcnt vmcnt(10)
	s_mov_b32 s7, 2
	s_mov_b32 s15, 0
	s_mov_b32 s13, 0xc000
	s_cmp_lg_u32 s14, 1
	s_cbranch_scc1 .LBB2_2
	s_barrier

.LBB3_6:
	v_add_u32_e32 v222, s22, v227
	ds_read_b64_tr_b16 v[194:195], v222 offset:24576
	ds_read_b64_tr_b16 v[196:197], v222 offset:25088
	s_waitcnt lgkmcnt(9)
	v_mfma_f32_32x32x16_f16 v[114:129], v[190:193], v[154:157], v[50:65]
	v_add_f32_e32 v98, v82, v83
	v_add_f32_e32 v98, v84, v98
	v_add_f32_e32 v98, v85, v98
	v_add_f32_e32 v98, v86, v98
	v_add_f32_e32 v98, v87, v98
	v_cvt_pk_f16_f32 v158, v82, v83
	v_cvt_pk_f16_f32 v159, v84, v85
	ds_read_b64_tr_b16 v[190:191], v222 offset:28672
	ds_read_b64_tr_b16 v[192:193], v222 offset:29184
	v_add_f32_e32 v82, v88, v98
	s_waitcnt lgkmcnt(10)
	v_mfma_f32_32x32x16_f16 v[98:113], v[186:189], v[154:157], v[50:65]
	v_add_f32_e32 v82, v89, v82
	v_add_f32_e32 v82, v90, v82
	v_add_f32_e32 v134, v91, v82
	v_cvt_pk_f16_f32 v160, v86, v87
	v_cvt_pk_f16_f32 v161, v88, v89
	ds_read_b64_tr_b16 v[82:83], v222 offset:25600
	ds_read_b64_tr_b16 v[84:85], v222 offset:26112
	s_waitcnt lgkmcnt(11)
	v_mfma_f32_32x32x16_f16 v[114:129], v[182:185], v[146:149], v[114:129]
	v_add_f32_e32 v86, v92, v134
	v_add_f32_e32 v86, v93, v86
	v_add_f32_e32 v86, v94, v86
	v_add_f32_e32 v134, v95, v86
	v_cvt_pk_f16_f32 v150, v90, v91
	v_cvt_pk_f16_f32 v151, v92, v93
	ds_read_b64_tr_b16 v[86:87], v222 offset:29696
	ds_read_b64_tr_b16 v[88:89], v222 offset:30208
	s_waitcnt lgkmcnt(12)
	v_mfma_f32_32x32x16_f16 v[98:113], v[178:181], v[146:149], v[98:113]
	v_add_f32_e32 v90, v96, v134
	v_add_f32_e32 v90, v97, v90
	v_add_f32_e32 v90, v66, v90
	v_add_f32_e32 v134, v67, v90
	v_cvt_pk_f16_f32 v152, v94, v95
	v_cvt_pk_f16_f32 v153, v96, v97
	ds_read_b64_tr_b16 v[90:91], v222 offset:26624
	ds_read_b64_tr_b16 v[92:93], v222 offset:27136
	s_waitcnt lgkmcnt(13)
	v_mfma_f32_32x32x16_f16 v[114:129], v[174:177], v[138:141], v[114:129]
	v_add_f32_e32 v94, v68, v134
	v_add_f32_e32 v94, v69, v94
	v_add_f32_e32 v94, v70, v94
	v_add_f32_e32 v94, v71, v94
	v_cvt_pk_f16_f32 v142, v66, v67
	v_cvt_pk_f16_f32 v143, v68, v69
	ds_read_b64_tr_b16 v[66:67], v222 offset:30720
	ds_read_b64_tr_b16 v[68:69], v222 offset:31232
	s_waitcnt lgkmcnt(14)
	v_mfma_f32_32x32x16_f16 v[98:113], v[170:173], v[138:141], v[98:113]
	v_add_f32_e32 v94, v72, v94
	v_add_f32_e32 v94, v73, v94
	v_add_f32_e32 v94, v74, v94
	v_add_f32_e32 v94, v75, v94
	v_cvt_pk_f16_f32 v144, v70, v71
	v_cvt_pk_f16_f32 v145, v72, v73
	ds_read_b64_tr_b16 v[70:71], v222 offset:27648
	ds_read_b64_tr_b16 v[72:73], v222 offset:28160
	s_waitcnt lgkmcnt(14)
	v_mfma_f32_32x32x16_f16 v[114:129], v[166:169], v[130:133], v[114:129]
	v_add_f32_e32 v94, v76, v94
	v_add_f32_e32 v94, v77, v94
	v_add_f32_e32 v94, v78, v94
	v_add_f32_e32 v94, v79, v94
	v_cvt_pk_f16_f32 v134, v74, v75
	v_cvt_pk_f16_f32 v135, v76, v77
	ds_read_b64_tr_b16 v[74:75], v222 offset:31744
	ds_read_b64_tr_b16 v[76:77], v222 offset:32256
	v_mfma_f32_32x32x16_f16 v[98:113], v[162:165], v[130:133], v[98:113]
	v_add_f32_e32 v94, v80, v94
	v_add_f32_e32 v94, v81, v94
	v_add_f32_e32 v94, 0, v94
	v_cvt_pk_f16_f32 v136, v78, v79
	v_cvt_pk_f16_f32 v137, v80, v81
	v_lshl_add_u64 v[78:79], v[204:205], 0, s[18:19]
	s_add_i32 s22, s29, s39
	s_mov_b32 s23, m0
	s_mov_b32 m0, s22
	s_nop 0
	global_load_lds_dwordx4 v[78:79], off
	s_mov_b32 m0, s23
	v_lshl_add_u64 v[78:79], v[202:203], 0, s[18:19]
	s_add_i32 s22, s27, s40
	s_mov_b32 s23, m0
	s_mov_b32 m0, s22
	s_nop 0
	global_load_lds_dwordx4 v[78:79], off
	s_mov_b32 m0, s23
	v_max_f32_e32 v78, v114, v115
	v_max3_f32 v79, v116, v117, v99
	v_max3_f32 v78, v78, v98, v100
	v_max3_f32 v78, v78, v101, v118
	v_max3_f32 v79, v79, v120, v121
	v_max3_f32 v78, v78, v119, v102
	v_max3_f32 v79, v79, v104, v105
	v_max3_f32 v78, v78, v103, v122
	v_max3_f32 v79, v79, v124, v125
	v_max3_f32 v78, v78, v123, v106
	v_max3_f32 v79, v79, v108, v109
	v_max3_f32 v78, v78, v107, v126
	v_max3_f32 v79, v79, v128, v129
	v_max3_f32 v78, v78, v127, v110
	v_max3_f32 v79, v79, v112, v113
	v_max3_f32 v78, v78, v111, v79
	v_mov_b32_e32 v79, v78
	s_nop 1
	v_permlane32_swap_b32_e32 v78, v79
	v_max_f32_e32 v78, v78, v79
	v_cmp_lt_f32_e32 vcc, s34, v78
	s_cmp_lg_u64 vcc, 0
	v_add_f32_e32 v222, v242, v94
	s_cselect_b64 s[22:23], -1, 0
	s_cbranch_vccnz .LBB3_14

.LBB3_9:
	s_add_i32 s22, s27, 0x2000
	s_cmpk_lg_i32 s27, 0x4000
	s_cselect_b32 s42, s22, 0
	v_add_u32_e32 v223, s29, v227
	ds_read_b64_tr_b16 v[166:167], v223 offset:24576
	ds_read_b64_tr_b16 v[168:169], v223 offset:25088
	s_waitcnt lgkmcnt(9)
	v_mfma_f32_32x32x16_f16 v[82:97], v[78:81], v[154:157], v[50:65]
	v_add_f32_e32 v66, v114, v115
	v_add_f32_e32 v66, v116, v66
	v_add_f32_e32 v66, v117, v66
	v_add_f32_e32 v66, v118, v66
	v_add_f32_e32 v66, v119, v66
	v_cvt_pk_f16_f32 v158, v114, v115
	v_cvt_pk_f16_f32 v159, v116, v117
	ds_read_b64_tr_b16 v[162:163], v223 offset:28672
	ds_read_b64_tr_b16 v[164:165], v223 offset:29184
	v_add_f32_e32 v66, v120, v66
	v_add_f32_e32 v66, v121, v66
	v_add_f32_e32 v66, v122, v66
	v_add_f32_e32 v134, v123, v66
	s_waitcnt lgkmcnt(10)
	v_mfma_f32_32x32x16_f16 v[66:81], v[190:193], v[154:157], v[50:65]
	v_cvt_pk_f16_f32 v160, v118, v119
	v_cvt_pk_f16_f32 v161, v120, v121
	ds_read_b64_tr_b16 v[114:115], v223 offset:25600
	ds_read_b64_tr_b16 v[116:117], v223 offset:26112
	s_waitcnt lgkmcnt(11)
	v_mfma_f32_32x32x16_f16 v[82:97], v[194:197], v[146:149], v[82:97]
	v_add_f32_e32 v118, v124, v134
	v_add_f32_e32 v118, v125, v118
	v_add_f32_e32 v118, v126, v118
	v_add_f32_e32 v134, v127, v118
	v_cvt_pk_f16_f32 v150, v122, v123
	v_cvt_pk_f16_f32 v151, v124, v125
	ds_read_b64_tr_b16 v[118:119], v223 offset:29696
	ds_read_b64_tr_b16 v[120:121], v223 offset:30208
	s_waitcnt lgkmcnt(12)
	v_mfma_f32_32x32x16_f16 v[66:81], v[186:189], v[146:149], v[66:81]
	v_add_f32_e32 v122, v128, v134
	v_add_f32_e32 v122, v129, v122
	v_add_f32_e32 v122, v98, v122
	v_add_f32_e32 v134, v99, v122
	v_cvt_pk_f16_f32 v152, v126, v127
	v_cvt_pk_f16_f32 v153, v128, v129
	ds_read_b64_tr_b16 v[122:123], v223 offset:26624
	ds_read_b64_tr_b16 v[124:125], v223 offset:27136
	s_waitcnt lgkmcnt(13)
	v_mfma_f32_32x32x16_f16 v[82:97], v[182:185], v[138:141], v[82:97]
	v_add_f32_e32 v126, v100, v134
	v_add_f32_e32 v126, v101, v126
	v_add_f32_e32 v126, v102, v126
	v_add_f32_e32 v126, v103, v126
	v_cvt_pk_f16_f32 v142, v98, v99
	v_cvt_pk_f16_f32 v143, v100, v101
	ds_read_b64_tr_b16 v[98:99], v223 offset:30720
	ds_read_b64_tr_b16 v[100:101], v223 offset:31232
	s_waitcnt lgkmcnt(14)
	v_mfma_f32_32x32x16_f16 v[66:81], v[178:181], v[138:141], v[66:81]
	v_add_f32_e32 v126, v104, v126
	v_add_f32_e32 v126, v105, v126
	v_add_f32_e32 v126, v106, v126
	v_add_f32_e32 v126, v107, v126
	v_cvt_pk_f16_f32 v144, v102, v103
	v_cvt_pk_f16_f32 v145, v104, v105
	ds_read_b64_tr_b16 v[102:103], v223 offset:27648
	ds_read_b64_tr_b16 v[104:105], v223 offset:28160
	s_waitcnt lgkmcnt(14)
	v_mfma_f32_32x32x16_f16 v[82:97], v[174:177], v[130:133], v[82:97]
	v_add_f32_e32 v126, v108, v126
	v_add_f32_e32 v126, v109, v126
	v_add_f32_e32 v126, v110, v126
	v_add_f32_e32 v126, v111, v126
	v_cvt_pk_f16_f32 v134, v106, v107
	v_cvt_pk_f16_f32 v135, v108, v109
	ds_read_b64_tr_b16 v[106:107], v223 offset:31744
	ds_read_b64_tr_b16 v[108:109], v223 offset:32256
	v_mfma_f32_32x32x16_f16 v[66:81], v[170:173], v[130:133], v[66:81]
	v_add_f32_e32 v126, v112, v126
	v_add_f32_e32 v126, v113, v126
	v_add_f32_e32 v126, 0, v126
	v_cvt_pk_f16_f32 v136, v110, v111
	v_cvt_pk_f16_f32 v137, v112, v113
	v_max_f32_e32 v110, v82, v83
	s_nop 5
	v_max3_f32 v111, v84, v85, v67
	v_max3_f32 v110, v110, v66, v68
	v_max3_f32 v110, v110, v69, v86
	v_max3_f32 v111, v111, v88, v89
	v_max3_f32 v110, v110, v87, v70
	v_max3_f32 v111, v111, v72, v73
	v_max3_f32 v110, v110, v71, v90
	v_max3_f32 v111, v111, v92, v93
	v_max3_f32 v110, v110, v91, v74
	v_max3_f32 v111, v111, v76, v77
	v_max3_f32 v110, v110, v75, v94
	v_max3_f32 v111, v111, v96, v97
	v_max3_f32 v110, v110, v95, v78
	v_max3_f32 v111, v111, v80, v81
	v_max3_f32 v110, v110, v79, v111
	v_mov_b32_e32 v111, v110
	s_nop 1
	v_permlane32_swap_b32_e32 v110, v111
	s_add_i32 s22, s27, s39
	s_mov_b32 s23, m0
	s_mov_b32 m0, s22
	s_nop 0
	global_load_lds_dwordx4 v[204:205], off
	s_mov_b32 m0, s23
	v_max_f32_e32 v110, v110, v111
	s_add_i32 s22, s42, s40
	s_mov_b32 s23, m0
	s_mov_b32 m0, s22
	s_nop 0
	global_load_lds_dwordx4 v[202:203], off
	s_mov_b32 m0, s23
	v_cmp_lt_f32_e32 vcc, s34, v110
	s_cmp_lg_u64 vcc, 0
	v_add_f32_e32 v242, v222, v126
	s_cselect_b64 s[22:23], -1, 0
	s_cbranch_vccnz .LBB3_17

.LBB3_27:
	v_max_f32_e32 v78, v114, v115
	v_max3_f32 v79, v116, v117, v99
	v_max3_f32 v78, v78, v98, v100
	v_max3_f32 v78, v78, v101, v118
	v_max3_f32 v79, v79, v120, v121
	v_max3_f32 v78, v78, v119, v102
	v_max3_f32 v79, v79, v104, v105
	v_max3_f32 v78, v78, v103, v122
	v_max3_f32 v79, v79, v124, v125
	v_max3_f32 v78, v78, v123, v106
	v_max3_f32 v79, v79, v108, v109
	v_max3_f32 v78, v78, v107, v126
	v_max3_f32 v79, v79, v128, v129
	v_max3_f32 v78, v78, v127, v110
	v_max3_f32 v79, v79, v112, v113
	v_max3_f32 v78, v78, v111, v79
	v_mov_b32_e32 v79, v78
	s_nop 1
	v_permlane32_swap_b32_e32 v78, v79
	v_max_f32_e32 v78, v78, v79
	v_cmp_lt_f32_e32 vcc, s34, v78
	s_cmp_lg_u64 vcc, 0
	v_add_f32_e32 v242, v242, v94
	s_cselect_b64 s[2:3], -1, 0
	s_cbranch_vccnz .LBB3_65

.LBB3_38:
	v_add_f32_e32 v242, v242, v106
	v_max_f32_e32 v106, v82, v83
	v_max3_f32 v107, v84, v85, v67
	v_max3_f32 v106, v106, v66, v68
	v_max3_f32 v106, v106, v69, v86
	v_max3_f32 v107, v107, v88, v89
	v_max3_f32 v106, v106, v87, v70
	v_max3_f32 v107, v107, v72, v73
	v_max3_f32 v106, v106, v71, v90
	v_max3_f32 v107, v107, v92, v93
	v_max3_f32 v106, v106, v91, v74
	v_max3_f32 v107, v107, v76, v77
	v_max3_f32 v106, v106, v75, v94
	v_max3_f32 v107, v107, v96, v97
	v_max3_f32 v106, v106, v95, v78
	v_max3_f32 v107, v107, v80, v81
	v_max3_f32 v106, v106, v79, v107
	v_mov_b32_e32 v107, v106
	s_nop 1
	v_permlane32_swap_b32_e32 v106, v107
	v_max_f32_e32 v106, v106, v107
	v_cmp_lt_f32_e32 vcc, s34, v106
	s_cmp_lg_u64 vcc, 0
	s_cselect_b64 s[28:29], -1, 0
	s_cbranch_vccnz .LBB3_68

.LBB3_72:
	v_add_u32_e32 v128, s43, v227
	ds_read_b64_tr_b16 v[118:119], v128 offset:24576
	ds_read_b64_tr_b16 v[120:121], v128 offset:25088
	v_add_f32_e32 v98, v82, v83
	v_add_f32_e32 v98, v84, v98
	v_add_f32_e32 v98, v85, v98
	v_add_f32_e32 v98, v86, v98
	v_add_f32_e32 v122, v87, v98
	s_waitcnt lgkmcnt(9)
	v_mfma_f32_32x32x16_f16 v[98:113], v[190:193], v[154:157], v[50:65]
	v_cvt_pk_f16_f32 v158, v82, v83
	v_cvt_pk_f16_f32 v159, v84, v85
	ds_read_b64_tr_b16 v[114:115], v128 offset:28672
	ds_read_b64_tr_b16 v[116:117], v128 offset:29184
	s_waitcnt lgkmcnt(10)
	v_mfma_f32_32x32x16_f16 v[50:65], v[186:189], v[154:157], v[50:65]
	v_add_f32_e32 v82, v88, v122
	v_add_f32_e32 v82, v89, v82
	v_add_f32_e32 v82, v90, v82
	v_add_f32_e32 v82, v91, v82
	v_cvt_pk_f16_f32 v160, v86, v87
	v_cvt_pk_f16_f32 v161, v88, v89
	ds_read_b64_tr_b16 v[122:123], v128 offset:25600
	ds_read_b64_tr_b16 v[124:125], v128 offset:26112
	s_waitcnt lgkmcnt(11)
	v_mfma_f32_32x32x16_f16 v[98:113], v[182:185], v[146:149], v[98:113]
	v_add_f32_e32 v82, v92, v82
	v_add_f32_e32 v82, v93, v82
	v_add_f32_e32 v82, v94, v82
	v_add_f32_e32 v82, v95, v82
	v_cvt_pk_f16_f32 v150, v90, v91
	v_cvt_pk_f16_f32 v151, v92, v93
	ds_read_b64_tr_b16 v[182:183], v128 offset:29696
	ds_read_b64_tr_b16 v[184:185], v128 offset:30208
	s_waitcnt lgkmcnt(12)
	v_mfma_f32_32x32x16_f16 v[50:65], v[178:181], v[146:149], v[50:65]
	v_add_f32_e32 v82, v96, v82
	v_add_f32_e32 v82, v97, v82
	v_add_f32_e32 v82, v66, v82
	v_add_f32_e32 v82, v67, v82
	v_cvt_pk_f16_f32 v152, v94, v95
	v_cvt_pk_f16_f32 v153, v96, v97
	ds_read_b64_tr_b16 v[154:155], v128 offset:26624
	ds_read_b64_tr_b16 v[156:157], v128 offset:27136
	s_waitcnt lgkmcnt(13)
	v_mfma_f32_32x32x16_f16 v[98:113], v[174:177], v[138:141], v[98:113]
	v_add_f32_e32 v82, v68, v82
	v_add_f32_e32 v82, v69, v82
	v_add_f32_e32 v82, v70, v82
	v_add_f32_e32 v82, v71, v82
	v_cvt_pk_f16_f32 v142, v66, v67
	v_cvt_pk_f16_f32 v143, v68, v69
	ds_read_b64_tr_b16 v[146:147], v128 offset:30720
	ds_read_b64_tr_b16 v[148:149], v128 offset:31232
	s_waitcnt lgkmcnt(14)
	v_mfma_f32_32x32x16_f16 v[50:65], v[170:173], v[138:141], v[50:65]
	v_add_f32_e32 v66, v72, v82
	v_add_f32_e32 v66, v73, v66
	v_add_f32_e32 v66, v74, v66
	v_add_f32_e32 v66, v75, v66
	v_cvt_pk_f16_f32 v144, v70, v71
	v_cvt_pk_f16_f32 v145, v72, v73
	ds_read_b64_tr_b16 v[138:139], v128 offset:27648
	ds_read_b64_tr_b16 v[140:141], v128 offset:28160
	s_waitcnt lgkmcnt(14)
	v_mfma_f32_32x32x16_f16 v[98:113], v[166:169], v[130:133], v[98:113]
	v_add_f32_e32 v66, v76, v66
	v_add_f32_e32 v66, v77, v66
	v_add_f32_e32 v66, v78, v66
	v_add_f32_e32 v66, v79, v66
	v_cvt_pk_f16_f32 v134, v74, v75
	v_cvt_pk_f16_f32 v135, v76, v77
	ds_read_b64_tr_b16 v[126:127], v128 offset:31744
	ds_read_b64_tr_b16 v[128:129], v128 offset:32256
	v_mfma_f32_32x32x16_f16 v[50:65], v[162:165], v[130:133], v[50:65]
	v_add_f32_e32 v66, v80, v66
	v_add_f32_e32 v66, v81, v66
	v_add_f32_e32 v82, 0, v66
	v_cvt_pk_f16_f32 v136, v78, v79
	v_cvt_pk_f16_f32 v137, v80, v81
	v_or_b32_e32 v66, 0xe0, v228
	v_cmp_le_u32_e32 vcc, v66, v219
	v_or_b32_e32 v68, 0xe1, v228
	v_or_b32_e32 v69, 0xe2, v228
	s_nop 2
	v_cndmask_b32_e32 v50, v241, v50, vcc
	v_cmp_lt_u32_e32 vcc, v230, v219
	v_or_b32_e32 v70, 0xe3, v228
	v_or_b32_e32 v71, 0xe8, v228
	v_cndmask_b32_e32 v67, v241, v99, vcc
	v_cmp_le_u32_e32 vcc, v230, v219
	v_or_b32_e32 v72, 0xe9, v228
	v_or_b32_e32 v73, 0xea, v228
	v_cndmask_b32_e32 v66, v241, v98, vcc
	v_cmp_le_u32_e32 vcc, v68, v219
	v_or_b32_e32 v68, 0xc2, v228
	v_or_b32_e32 v74, 0xeb, v228
	v_cndmask_b32_e32 v51, v241, v51, vcc
	v_cmp_le_u32_e32 vcc, v68, v219
	v_or_b32_e32 v75, 0xf0, v228
	v_or_b32_e32 v76, 0xf1, v228
	v_cndmask_b32_e32 v68, v241, v100, vcc
	v_cmp_le_u32_e32 vcc, v69, v219
	v_or_b32_e32 v69, 0xc3, v228
	v_or_b32_e32 v77, 0xf2, v228
	v_cndmask_b32_e32 v52, v241, v52, vcc
	v_cmp_le_u32_e32 vcc, v69, v219
	v_or_b32_e32 v78, 0xf3, v228
	v_or_b32_e32 v79, 0xf8, v228
	v_cndmask_b32_e32 v69, v241, v101, vcc
	v_cmp_le_u32_e32 vcc, v70, v219
	v_or_b32_e32 v70, 0xc8, v228
	v_or_b32_e32 v80, 0xf9, v228
	v_cndmask_b32_e32 v53, v241, v53, vcc
	v_cmp_le_u32_e32 vcc, v70, v219
	v_or_b32_e32 v81, 0xfa, v228
	v_or_b32_e32 v83, 0xfb, v228
	v_cndmask_b32_e32 v70, v241, v102, vcc
	v_cmp_le_u32_e32 vcc, v71, v219
	v_or_b32_e32 v71, 0xc9, v228
	v_max_f32_e32 v84, v66, v66
	v_cndmask_b32_e32 v54, v241, v54, vcc
	v_cmp_le_u32_e32 vcc, v71, v219
	v_add_f32_e32 v98, v242, v82
	s_nop 0
	v_cndmask_b32_e32 v71, v241, v103, vcc
	v_cmp_le_u32_e32 vcc, v72, v219
	v_or_b32_e32 v72, 0xca, v228
	s_nop 0
	v_cndmask_b32_e32 v55, v241, v55, vcc
	v_cmp_le_u32_e32 vcc, v72, v219
	s_nop 1
	v_cndmask_b32_e32 v72, v241, v104, vcc
	v_cmp_le_u32_e32 vcc, v73, v219
	v_or_b32_e32 v73, 0xcb, v228
	s_nop 0
	v_cndmask_b32_e32 v56, v241, v56, vcc
	v_cmp_le_u32_e32 vcc, v73, v219
	s_nop 1
	v_cndmask_b32_e32 v73, v241, v105, vcc
	v_cmp_le_u32_e32 vcc, v74, v219
	v_or_b32_e32 v74, 0xd0, v228
	s_nop 0
	v_cndmask_b32_e32 v57, v241, v57, vcc
	v_cmp_le_u32_e32 vcc, v74, v219
	s_nop 1
	v_cndmask_b32_e32 v74, v241, v106, vcc
	v_cmp_le_u32_e32 vcc, v75, v219
	v_or_b32_e32 v75, 0xd1, v228
	s_nop 0
	v_cndmask_b32_e32 v58, v241, v58, vcc
	v_cmp_le_u32_e32 vcc, v75, v219
	s_nop 1
	v_cndmask_b32_e32 v75, v241, v107, vcc
	v_cmp_le_u32_e32 vcc, v76, v219
	v_or_b32_e32 v76, 0xd2, v228
	s_nop 0
	v_cndmask_b32_e32 v59, v241, v59, vcc
	v_cmp_le_u32_e32 vcc, v76, v219
	s_nop 1
	v_cndmask_b32_e32 v76, v241, v108, vcc
	v_cmp_le_u32_e32 vcc, v77, v219
	v_or_b32_e32 v77, 0xd3, v228
	s_nop 0
	v_cndmask_b32_e32 v60, v241, v60, vcc
	v_cmp_le_u32_e32 vcc, v77, v219
	s_nop 1
	v_cndmask_b32_e32 v77, v241, v109, vcc
	v_cmp_le_u32_e32 vcc, v78, v219
	v_or_b32_e32 v78, 0xd8, v228
	s_nop 0
	v_cndmask_b32_e32 v61, v241, v61, vcc
	v_cmp_le_u32_e32 vcc, v78, v219
	s_nop 1
	v_cndmask_b32_e32 v78, v241, v110, vcc
	v_cmp_le_u32_e32 vcc, v79, v219
	v_or_b32_e32 v79, 0xd9, v228
	s_nop 0
	v_cndmask_b32_e32 v62, v241, v62, vcc
	v_cmp_le_u32_e32 vcc, v79, v219
	s_nop 1
	v_cndmask_b32_e32 v79, v241, v111, vcc
	v_cmp_le_u32_e32 vcc, v80, v219
	v_or_b32_e32 v80, 0xda, v228
	s_nop 0
	v_cndmask_b32_e32 v63, v241, v63, vcc
	v_cmp_le_u32_e32 vcc, v80, v219
	s_nop 1
	v_cndmask_b32_e32 v80, v241, v112, vcc
	v_cmp_le_u32_e32 vcc, v81, v219
	v_or_b32_e32 v81, 0xdb, v228
	s_nop 0
	v_cndmask_b32_e32 v64, v241, v64, vcc
	v_cmp_le_u32_e32 vcc, v81, v219
	s_nop 1
	v_cndmask_b32_e32 v81, v241, v113, vcc
	v_cmp_le_u32_e32 vcc, v83, v219
	v_max_f32_e32 v83, v67, v67
	v_max_f32_e32 v83, v84, v83
	v_max3_f32 v84, v68, v69, v51
	v_max3_f32 v83, v83, v50, v52
	v_max3_f32 v83, v83, v53, v70
	v_max3_f32 v84, v84, v72, v73
	v_max3_f32 v83, v83, v71, v54
	v_max3_f32 v84, v84, v56, v57
	v_max3_f32 v83, v83, v55, v74
	v_max3_f32 v84, v84, v76, v77
	v_max3_f32 v83, v83, v75, v58
	v_max3_f32 v84, v84, v60, v61
	v_cndmask_b32_e32 v65, v241, v65, vcc
	v_max3_f32 v83, v83, v59, v78
	v_max3_f32 v84, v84, v80, v81
	v_max3_f32 v83, v83, v79, v62
	v_max3_f32 v84, v84, v64, v65
	v_max3_f32 v82, v83, v63, v84
	v_mov_b32_e32 v83, v82
	s_nop 1
	v_permlane32_swap_b32_e32 v82, v83
	v_max_f32_e32 v82, v82, v83
	v_cmp_lt_f32_e32 vcc, s34, v82
	s_cmp_lg_u64 vcc, 0
	s_cselect_b64 s[2:3], -1, 0
	s_cbranch_vccnz .LBB3_77
